# drop hipcc vmcnt(0) drains: DA tile barrier keeps tile j+1 DMA in flight; epilogue bias wait vmcnt(8)
# speedup vs baseline: 1.0029x; 1.0029x over previous
; __device__ __forceinline__ void da_unit(LAS unsigned char* lds, const bf16* __restrict__ Q, const bf16* __restrict__ Kp, const bf16* __restrict__ Vp, const float* __restrict__ gda, float lam, ...
;     ...
;     { const bf16* Qw = Q + (size_t)(m0 + 32 * rg + r32) * HW + h * 128 + comp * 64 + hi * 8;
; #pragma unroll
;       for (int d0 = 0; d0 < 4; ++d0) qr[d0] = *(const bf16x8*)(Qw + d0 * 16); }
;     const bf16* Kh = Kp + (size_t)(b * LPB) * HW + h * 128; const bf16* Vh = Vp + (size_t)(b * LPB) * HW + h * 128;
;     const int vb0 = (int)(unsigned)(uintptr_t)V_lds + v_rd_base(lane);
;     const int NT = 2 * qt + 3, NTw = 2 * qt + 2 + (rg >> 1);
;     const AttDma dm = att_dma_init(wave, lane);
;     att_dma(dm, Kh, Vh, 0, K_lds, V_lds, wave);
;     att_dma(dm, Kh, Vh, 64, K_lds + SHM_T, V_lds + SHM_T, wave);
;     int kbuf = 0;
;     float m_reg = 0.f, l_reg = 0.f; f32x16 o[4];
;     f32x16 mneg;
; #pragma unroll
;     for (int r = 0; r < 16; ++r) mneg[r] = 0.f;
; #pragma unroll
;     for (int d = 0; d < 4; ++d)
; #pragma unroll
;         for (int r = 0; r < 16; ++r) o[d][r] = 0.f;
;     bf16x8 pa0, pa1, pa2, pa3; bool pend = false; int pbuf = 0, vbuf = 0;
; #pragma unroll
;     for (int q = 0; q < 8; ++q) { pa0[q] = 0; pa1[q] = 0; pa2[q] = 0; pa3[q] = 0; }
;     for (int j = 0; j < NT; ++j) {
;         const int buf = kbuf;
;         if (j + 1 < NT) asm volatile("s_waitcnt vmcnt(4)" ::: "memory"); else asm volatile("s_waitcnt vmcnt(0)" ::: "memory");
;         __syncthreads();
;         if (j + 2 < NT) att_dma(dm, Kh, Vh, (j + 2) * 64, K_lds + (kbuf == 0 ? 2 : kbuf - 1) * SHM_T, V_lds + ((vbuf + 2) & 3) * SHM_T, wave);
;         if (comp == 1 && pend) { pv_pipe(o, vb0 + pbuf * SHM_T, pa0, pa1, pa2, pa3); pend = false; }
;         if (j < NTw) {
;             f32x16 p0 = mneg, p1 = mneg;
;             { const LAS unsigned char* Ks = K_lds + buf * SHM_T; bf16x8 kb0[4], kb1[4];
; #pragma unroll
;               for (int d0 = 0; d0 < 4; ++d0) { const int cb = (comp * 64 + d0 * 16 + hi * 8) * 2;
;                   kb0[d0] = *(const LAS bf16x8*)(Ks + KSWZ(r32, cb)); kb1[d0] = *(const LAS bf16x8*)(Ks + KSWZ(32 + r32, cb)); }
;               SBAR();
; #pragma unroll
;               for (int d0 = 0; d0 < 4; ++d0) { p0 = __builtin_amdgcn_mfma_f32_32x32x16_bf16(kb0[d0], qr[d0], p0, 0, 0, 0); p1 = __builtin_amdgcn_mfma_f32_32x32x16_bf16(kb1[d0], qr[d0], p1, 0, 0, 0); } }
.LBB0_569:
	s_and_b32 s4, s95, 2
	s_or_b32 s96, s88, s4
	s_bitcmp0_b32 s95, 0
	s_cselect_b32 s73, s87, s89
	s_lshl_b32 s4, s73, 7
	s_or_b32 s72, s4, s90
	v_or_b32_e32 v2, s72, v131
	v_ashrrev_i32_e32 v3, 31, v2
	v_lshlrev_b64 v[2:3], 11, v[2:3]
	s_lshl_b32 s16, s96, 8
	v_lshl_add_u64 v[2:3], s[2:3], 0, v[2:3]
	s_add_u32 s4, s91, s16
	v_lshl_add_u64 v[2:3], v[2:3], 0, s[16:17]
	s_mov_b32 s69, s17
	s_addc_u32 s5, s92, 0
	v_lshl_add_u64 v[2:3], v[2:3], 0, s[68:69]
	s_add_u32 s64, s93, s16
	s_mov_b32 m0, s76
	v_lshl_add_u64 v[2:3], v[2:3], 0, v[146:147]
	s_addc_u32 s8, s94, 0
	s_and_b32 s5, s5, 0xffff
	global_load_dwordx4 v[114:117], v[2:3], off
	global_load_dwordx4 v[118:121], v[2:3], off offset:32
	global_load_dwordx4 v[122:125], v[2:3], off offset:64
	global_load_dwordx4 v[126:129], v[2:3], off offset:96
	s_and_b32 s65, s8, 0xffff
	s_mov_b32 s66, s6
	s_mov_b32 s67, s7
	buffer_load_dwordx4 v135, s[4:7], 0 offen lds
	s_mov_b32 m0, s57
	v_add_u32_e32 v2, v172, v173
	buffer_load_dwordx4 v137, s[64:67], 0 offen lds
	s_mov_b32 m0, s77
	v_add_u32_e32 v6, v172, v174
	buffer_load_dwordx4 v139, s[4:7], 0 offen lds
	s_mov_b32 m0, s58
	s_waitcnt vmcnt(29)
	v_add_u32_e32 v10, v172, v175
	buffer_load_dwordx4 v141, s[64:67], 0 offen lds
	s_mov_b32 m0, s78
	s_waitcnt vmcnt(29)
	v_add_u32_e32 v14, v172, v176
	buffer_load_dwordx4 v135, s[4:7], s7 offen lds
	s_mov_b32 m0, s79
	s_nop 0
	buffer_load_dwordx4 v137, s[64:67], s7 offen lds
	s_mov_b32 m0, s80
	s_nop 0
	buffer_load_dwordx4 v139, s[4:7], s7 offen lds
	s_mov_b32 m0, s81
	s_nop 0
	buffer_load_dwordx4 v141, s[64:67], s7 offen lds
	s_mov_b32 m0, s83
	s_waitcnt vmcnt(4)
	s_barrier
	buffer_load_dwordx4 v135, s[4:7], s85 offen lds
	s_mov_b32 m0, s33
	s_nop 0
	buffer_load_dwordx4 v137, s[64:67], s85 offen lds
	s_mov_b32 m0, s84
	s_nop 0
	buffer_load_dwordx4 v139, s[4:7], s85 offen lds
	s_mov_b32 m0, s59
	s_nop 0
	buffer_load_dwordx4 v141, s[64:67], s85 offen lds
	ds_read_b128 v[2:5], v2
	ds_read_b128 v[6:9], v6
	ds_read_b128 v[10:13], v10
	ds_read_b128 v[34:37], v14
	s_waitcnt lgkmcnt(3)
	v_mfma_f32_32x32x16_bf16 v[18:33], v[2:5], v[114:117], 0
	s_mov_b32 s8, 0xff800000
	s_mov_b32 s16, s17
	s_mov_b32 s18, s17
	s_mov_b32 s19, s17
	s_mov_b32 s20, s17
	s_mov_b32 s21, s17
	s_mov_b32 s22, s17
	s_waitcnt lgkmcnt(2)
	v_mfma_f32_32x32x16_bf16 v[18:33], v[6:9], v[118:121], v[18:33]
	s_mov_b32 s23, s17
	s_mov_b32 s24, s17
	s_mov_b32 s25, s17
	s_mov_b32 s26, s17
	s_mov_b32 s27, s17
	s_mov_b32 s28, s17
	s_mov_b32 s29, s17
	s_waitcnt lgkmcnt(1)
	v_mfma_f32_32x32x16_bf16 v[18:33], v[10:13], v[122:125], v[18:33]
	s_mov_b32 s30, s17
	s_mov_b32 s31, s17
	v_mov_b64_e32 v[2:3], s[16:17]
	v_mov_b64_e32 v[16:17], s[30:31]
	v_mov_b64_e32 v[4:5], s[18:19]
	v_mov_b64_e32 v[6:7], s[20:21]
	v_mov_b64_e32 v[8:9], s[22:23]
	s_waitcnt lgkmcnt(0)
	v_mfma_f32_32x32x16_bf16 v[18:33], v[34:37], v[126:129], v[18:33]
	v_mov_b64_e32 v[10:11], s[24:25]
	v_mov_b64_e32 v[12:13], s[26:27]
	v_mov_b64_e32 v[14:15], s[28:29]
	v_mov_b64_e32 v[48:49], v[16:17]
	v_mov_b64_e32 v[64:65], v[16:17]
	s_and_b64 vcc, exec, s[44:45]
	v_mov_b64_e32 v[46:47], v[14:15]
	s_nop 4
	v_max3_f32 v18, v26, s8, v27
	v_max3_f32 v18, v18, v28, v29
	v_max3_f32 v18, v18, v30, v31
	v_max3_f32 v67, v18, v32, v33
	v_mov_b32_e32 v18, v67
	s_nop 1
	v_permlane32_swap_b32_e32 v67, v18
	v_sub_f32_e32 v18, 0xff800000, v67
	v_exp_f32_e32 v18, v18
	v_sub_f32_e32 v20, v27, v67
	v_sub_f32_e32 v19, v26, v67
	v_exp_f32_e32 v19, v19
	v_add_f32_e32 v27, 0, v18
	v_add_f32_e32 v27, v18, v27
	v_add_f32_e32 v27, v18, v27
	v_add_f32_e32 v27, v18, v27
	v_add_f32_e32 v27, v18, v27
	v_add_f32_e32 v27, v18, v27
	v_add_f32_e32 v27, v18, v27
	v_add_f32_e32 v27, v18, v27
	v_add_f32_e32 v27, v18, v27
	v_add_f32_e32 v27, v18, v27
	v_add_f32_e32 v27, v18, v27
	v_add_f32_e32 v27, v18, v27
	v_add_f32_e32 v27, v18, v27
	v_add_f32_e32 v27, v18, v27
	v_add_f32_e32 v27, v18, v27
	v_add_f32_e32 v27, v18, v27
	v_add_f32_e32 v27, v18, v27
	v_add_f32_e32 v27, v18, v27
	v_add_f32_e32 v27, v18, v27
	v_add_f32_e32 v27, v18, v27
	v_add_f32_e32 v27, v18, v27
	v_sub_f32_e32 v21, v28, v67
	v_exp_f32_e32 v20, v20
	v_add_f32_e32 v27, v18, v27
	v_sub_f32_e32 v22, v29, v67
	v_exp_f32_e32 v21, v21
	v_add_f32_e32 v27, v18, v27
	v_sub_f32_e32 v23, v30, v67
	v_exp_f32_e32 v22, v22
	v_add_f32_e32 v27, v18, v27
	v_sub_f32_e32 v24, v31, v67
	v_exp_f32_e32 v23, v23
	v_add_f32_e32 v27, v19, v27
	v_sub_f32_e32 v25, v32, v67
	v_exp_f32_e32 v24, v24
	v_add_f32_e32 v27, v20, v27
	v_sub_f32_e32 v26, v33, v67
	v_exp_f32_e32 v25, v25
	v_add_f32_e32 v27, v21, v27
	v_exp_f32_e32 v26, v26
	v_add_f32_e32 v27, v22, v27
	v_add_f32_e32 v27, v23, v27
	v_add_f32_e32 v27, v24, v27
	v_add_f32_e32 v27, v25, v27
	v_add_f32_e32 v66, v26, v27
	v_mov_b32_e32 v27, v66
	v_cvt_pk_bf16_f32 v86, v18, v18
	s_nop 0
	v_permlane32_swap_b32_e32 v66, v27
	v_mov_b32_e32 v88, v86
	s_nop 1
	v_permlane32_swap_b32_e32 v86, v88
	v_cvt_pk_bf16_f32 v82, v19, v20
	v_cvt_pk_bf16_f32 v83, v21, v22
	v_cvt_pk_bf16_f32 v84, v23, v24
	v_cvt_pk_bf16_f32 v85, v25, v26
	v_mov_b64_e32 v[32:33], v[16:17]
	v_mov_b32_e32 v87, v86
	v_mov_b32_e32 v89, v88
	v_permlane32_swap_b32_e32 v82, v84
	v_permlane32_swap_b32_e32 v83, v85
	v_mov_b64_e32 v[30:31], v[14:15]
	v_mov_b64_e32 v[28:29], v[12:13]
	v_mov_b64_e32 v[26:27], v[10:11]
	v_mov_b64_e32 v[24:25], v[8:9]
	v_mov_b64_e32 v[22:23], v[6:7]
	v_mov_b64_e32 v[20:21], v[4:5]
	v_mov_b64_e32 v[18:19], v[2:3]
	v_mov_b64_e32 v[44:45], v[12:13]
	v_mov_b64_e32 v[42:43], v[10:11]
	v_mov_b64_e32 v[40:41], v[8:9]
	v_mov_b64_e32 v[38:39], v[6:7]
	v_mov_b64_e32 v[36:37], v[4:5]
	v_mov_b64_e32 v[34:35], v[2:3]
	v_mov_b64_e32 v[62:63], v[14:15]
	v_mov_b64_e32 v[60:61], v[12:13]
	v_mov_b64_e32 v[58:59], v[10:11]
	v_mov_b64_e32 v[56:57], v[8:9]
	v_mov_b64_e32 v[54:55], v[6:7]
	v_mov_b64_e32 v[52:53], v[4:5]
	v_mov_b64_e32 v[50:51], v[2:3]
	s_cbranch_vccz .LBB0_571
; #define SBAR() __builtin_amdgcn_sched_barrier(0)
; #define ATT_RDK(X, KS) do { X##0 = tr_read<v_rd_off(0, KS, 0)>(vb); X##1 = tr_read<v_rd_off(0, KS, 1)>(vb); X##2 = tr_read<v_rd_off(1, KS, 0)>(vb); X##3 = tr_read<v_rd_off(1, KS, 1)>(vb); \
;     X##4 = tr_read<v_rd_off(2, KS, 0)>(vb); X##5 = tr_read<v_rd_off(2, KS, 1)>(vb); X##6 = tr_read<v_rd_off(3, KS, 0)>(vb); X##7 = tr_read<v_rd_off(3, KS, 1)>(vb); } while (0)
; #define ATT_MMAK(PA, X) do { o[0] = __builtin_amdgcn_mfma_f32_32x32x16_bf16(PA, ATT_PKV(X##0, X##1), o[0], 0, 0, 0); o[1] = __builtin_amdgcn_mfma_f32_32x32x16_bf16(PA, ATT_PKV(X##2, X##3), o[1], 0, 0, 0); \
;     o[2] = __builtin_amdgcn_mfma_f32_32x32x16_bf16(PA, ATT_PKV(X##4, X##5), o[2], 0, 0, 0); o[3] = __builtin_amdgcn_mfma_f32_32x32x16_bf16(PA, ATT_PKV(X##6, X##7), o[3], 0, 0, 0); } while (0)
; __device__ __forceinline__ void pv_pipe(f32x16* o, int vb, bf16x8 pa0, bf16x8 pa1, bf16x8 pa2, bf16x8 pa3) {
;     s16x4 a0, a1, a2, a3, a4, a5, a6, a7, b0, b1, b2, b3, b4, b5, b6, b7;
;     SBAR(); ATT_RDK(a, 0); ATT_RDK(b, 1);
;     asm volatile("s_waitcnt lgkmcnt(8)" ::: "memory"); SBAR(); ATT_MMAK(pa0, a);
;     SBAR(); ATT_RDK(a, 2);
;     asm volatile("s_waitcnt lgkmcnt(8)" ::: "memory"); SBAR(); ATT_MMAK(pa1, b);
;     SBAR(); ATT_RDK(b, 3);
;     asm volatile("s_waitcnt lgkmcnt(8)" ::: "memory"); SBAR(); ATT_MMAK(pa2, a);
;     asm volatile("s_waitcnt lgkmcnt(0)" ::: "memory"); SBAR(); ATT_MMAK(pa3, b);
; }
	ds_read_b64_tr_b16 v[2:3], v169 offset:0
	ds_read_b64_tr_b16 v[4:5], v169 offset:0x800
	ds_read_b64_tr_b16 v[18:19], v169 offset:0x200
	ds_read_b64_tr_b16 v[20:21], v169 offset:0xa00
	ds_read_b64_tr_b16 v[34:35], v169 offset:0x400
	ds_read_b64_tr_b16 v[36:37], v169 offset:0xc00
	ds_read_b64_tr_b16 v[50:51], v169 offset:0x600
	ds_read_b64_tr_b16 v[52:53], v169 offset:0xe00
	ds_read_b64_tr_b16 v[68:69], v169 offset:0x1000
	ds_read_b64_tr_b16 v[70:71], v169 offset:0x1800
	ds_read_b64_tr_b16 v[72:73], v169 offset:0x1200
	ds_read_b64_tr_b16 v[74:75], v169 offset:0x1a00
	ds_read_b64_tr_b16 v[76:77], v169 offset:0x1400
	ds_read_b64_tr_b16 v[78:79], v169 offset:0x1c00
	ds_read_b64_tr_b16 v[90:91], v169 offset:0x1600
	ds_read_b64_tr_b16 v[92:93], v169 offset:0x1e00
	s_waitcnt lgkmcnt(8)
	s_nop 0
	v_mfma_f32_32x32x16_bf16 v[2:17], v[86:89], v[2:5], 0
	v_mfma_f32_32x32x16_bf16 v[18:33], v[86:89], v[18:21], 0
	v_mfma_f32_32x32x16_bf16 v[34:49], v[86:89], v[34:37], 0
	v_mfma_f32_32x32x16_bf16 v[50:65], v[86:89], v[50:53], 0
	ds_read_b64_tr_b16 v[94:95], v169 offset:0x2000
	ds_read_b64_tr_b16 v[96:97], v169 offset:0x2800
	ds_read_b64_tr_b16 v[98:99], v169 offset:0x2200
	ds_read_b64_tr_b16 v[100:101], v169 offset:0x2a00
	ds_read_b64_tr_b16 v[102:103], v169 offset:0x2400
	ds_read_b64_tr_b16 v[104:105], v169 offset:0x2c00
	ds_read_b64_tr_b16 v[106:107], v169 offset:0x2600
	ds_read_b64_tr_b16 v[108:109], v169 offset:0x2e00
	s_waitcnt lgkmcnt(8)
	v_mfma_f32_32x32x16_bf16 v[2:17], v[86:89], v[68:71], v[2:17]
	v_mfma_f32_32x32x16_bf16 v[18:33], v[86:89], v[72:75], v[18:33]
	v_mfma_f32_32x32x16_bf16 v[34:49], v[86:89], v[76:79], v[34:49]
	v_mfma_f32_32x32x16_bf16 v[50:65], v[86:89], v[90:93], v[50:65]
	ds_read_b64_tr_b16 v[68:69], v169 offset:0x3000
	ds_read_b64_tr_b16 v[70:71], v169 offset:0x3800
	ds_read_b64_tr_b16 v[72:73], v169 offset:0x3200
	ds_read_b64_tr_b16 v[74:75], v169 offset:0x3a00
	ds_read_b64_tr_b16 v[76:77], v169 offset:0x3400
	ds_read_b64_tr_b16 v[78:79], v169 offset:0x3c00
	ds_read_b64_tr_b16 v[90:91], v169 offset:0x3600
	ds_read_b64_tr_b16 v[92:93], v169 offset:0x3e00
	s_waitcnt lgkmcnt(8)
	v_mfma_f32_32x32x16_bf16 v[2:17], v[86:89], v[94:97], v[2:17]
	s_waitcnt lgkmcnt(0)
	v_mfma_f32_32x32x16_bf16 v[18:33], v[86:89], v[98:101], v[18:33]
	v_mfma_f32_32x32x16_bf16 v[34:49], v[86:89], v[102:105], v[34:49]
	v_mfma_f32_32x32x16_bf16 v[50:65], v[86:89], v[106:109], v[50:65]
	v_mfma_f32_32x32x16_bf16 v[2:17], v[82:85], v[68:71], v[2:17]
	v_mfma_f32_32x32x16_bf16 v[18:33], v[82:85], v[72:75], v[18:33]
	v_mfma_f32_32x32x16_bf16 v[34:49], v[82:85], v[76:79], v[34:49]
	v_mfma_f32_32x32x16_bf16 v[50:65], v[82:85], v[90:93], v[50:65]

; __device__ __forceinline__ void da_unit(LAS unsigned char* lds, const bf16* __restrict__ Q, const bf16* __restrict__ Kp, const bf16* __restrict__ Vp, const float* __restrict__ gda, float lam, ...
;     ...
;         const int buf = kbuf;
;         if (j + 1 < NT) asm volatile("s_waitcnt vmcnt(4)" ::: "memory"); else asm volatile("s_waitcnt vmcnt(0)" ::: "memory");
;         __syncthreads();
;         if (j + 2 < NT) att_dma(dm, Kh, Vh, (j + 2) * 64, K_lds + (kbuf == 0 ? 2 : kbuf - 1) * SHM_T, V_lds + ((vbuf + 2) & 3) * SHM_T, wave);
;         if (comp == 1 && pend) { pv_pipe(o, vb0 + pbuf * SHM_T, pa0, pa1, pa2, pa3); pend = false; }
.LBB0_579:
	s_add_i32 s8, s27, 5
	s_cmp_ge_u32 s8, s24
	s_barrier
	s_cbranch_scc1 .LBB0_582
	s_lshl_b32 s8, s23, 14
	s_addk_i32 s8, 0xc000
	s_cmp_lg_u32 s23, 0
	s_cselect_b32 s8, s8, 0x8000
	s_lshl_b32 s9, s29, 14
	s_xor_b32 s9, s9, 0x8000
	s_add_i32 s8, s76, s8
	s_mov_b32 m0, s8
	s_add_i32 s9, s57, s9
	buffer_load_dwordx4 v135, s[4:7], s28 offen lds
	s_mov_b32 s66, s6
	s_mov_b32 s67, s7
	s_mov_b32 m0, s9
	s_nop 0
	buffer_load_dwordx4 v137, s[64:67], s28 offen lds
	s_add_i32 m0, s8, 0x2000
	s_nop 0
	buffer_load_dwordx4 v139, s[4:7], s28 offen lds
	s_add_i32 m0, s9, 0x2000
	s_nop 0
	buffer_load_dwordx4 v141, s[64:67], s28 offen lds
	s_and_b64 s[8:9], s[12:13], s[18:19]
	s_andn2_b64 vcc, exec, s[8:9]
	s_cbranch_vccz .LBB0_583

; #define LAS __attribute__((address_space(3)))
;     __device__ __forceinline__ void operator()(const f32x4 (&acc)[2][2][4][2], const Unit& u, int wr, int wc, int fr, int fq, float b1, LAS float* bx) const {
;         const int row0 = u.pm * BM + wr * 64 + fr, col0 = u.pn * HALF + wc * 32 + 8 * fq;
;         bx[threadIdx.x & 63] = b1;
;         const f32x4 g0 = *(const LAS f32x4*)(bx + 8 * fq), g1 = *(const LAS f32x4*)(bx + 8 * fq + 4), u0 = *(const LAS f32x4*)(bx + 32 + 8 * fq), u1 = *(const LAS f32x4*)(bx + 36 + 8 * fq);
; #pragma unroll
;         for (int ai = 0; ai < 2; ++ai)
; #pragma unroll
;             for (int m = 0; m < 4; ++m) {
;                 bf16* rowp = act + (size_t)(row0 + ai * HALF + m * 16) * DM + col0;
;                 float o[8];
; #pragma unroll
;                 for (int n = 0; n < 2; ++n)
; #pragma unroll
;                     for (int j = 0; j < 4; j += 2) {
;                         const f32x4 gb = n ? g1 : g0, ub = n ? u1 : u0;
;                         const f32x2_t hg = f32x2_t{acc[ai][0][m][n][j], acc[ai][0][m][n][j + 1]} + f32x2_t{gb[j], gb[j + 1]};
;                         const f32x2_t hu = f32x2_t{acc[ai][1][m][n][j], acc[ai][1][m][n][j + 1]} + f32x2_t{ub[j], ub[j + 1]};
;                         const f32x2_t gt = {fminf(hg[0], 7.0f), fminf(hg[1], 7.0f)}, up = {fminf(fmaxf(hu[0], -7.0f), 7.0f), fminf(fmaxf(hu[1], -7.0f), 7.0f)};
;                         const f32x2_t t = gt * (-1.702f * 1.4426950408889634f);
.LBB0_1248:
	s_waitcnt vmcnt(8)
	ds_write_b32 v168, v130
	ds_read_b128 v[142:145], v169
	ds_read_b128 v[134:137], v169 offset:16
	ds_read_b128 v[138:141], v169 offset:128
	ds_read_b128 v[130:133], v169 offset:144
	v_lshl_add_u32 v154, s84, 8, v1
	s_waitcnt lgkmcnt(3)
	v_pk_add_f32 v[128:129], v[128:129], v[144:145]
	v_pk_add_f32 v[126:127], v[126:127], v[142:143]
	v_min_f32_e32 v128, 0x40e00000, v128
	v_min_f32_e32 v129, 0x40e00000, v129
	v_pk_mul_f32 v[178:179], v[128:129], s[26:27] op_sel_hi:[1,0]
	s_waitcnt lgkmcnt(1)
	v_pk_add_f32 v[118:119], v[118:119], v[138:139]
	v_exp_f32_e32 v178, v178
	v_exp_f32_e32 v179, v179
	v_min_f32_e32 v126, 0x40e00000, v126
	v_min_f32_e32 v127, 0x40e00000, v127
	v_med3_f32 v118, v118, s63, v167
	v_med3_f32 v119, v119, s63, v167
	v_pk_mul_f32 v[176:177], v[126:127], s[26:27] op_sel_hi:[1,0]
	v_pk_fma_f32 v[118:119], v[126:127], v[118:119], v[126:127]
	v_pk_add_f32 v[126:127], v[178:179], 1.0 op_sel_hi:[1,0]
	v_pk_add_f32 v[120:121], v[120:121], v[140:141]
	v_rcp_f32_e32 v126, v126
	v_rcp_f32_e32 v127, v127
	v_med3_f32 v120, v120, s63, v167
	v_med3_f32 v121, v121, s63, v167
	v_pk_add_f32 v[122:123], v[122:123], v[134:135]
	v_pk_fma_f32 v[120:121], v[128:129], v[120:121], v[128:129]
	v_min_f32_e32 v122, 0x40e00000, v122
	v_min_f32_e32 v123, 0x40e00000, v123
	v_pk_mul_f32 v[120:121], v[120:121], v[126:127]
	v_pk_mul_f32 v[126:127], v[122:123], s[26:27] op_sel_hi:[1,0]
	v_exp_f32_e32 v176, v176
	v_exp_f32_e32 v126, v126
	v_exp_f32_e32 v127, v127
	v_exp_f32_e32 v177, v177
	v_pk_add_f32 v[124:125], v[124:125], v[136:137]
	s_waitcnt lgkmcnt(0)
	v_pk_add_f32 v[110:111], v[110:111], v[130:131]
	v_min_f32_e32 v124, 0x40e00000, v124
	v_min_f32_e32 v125, 0x40e00000, v125
	v_pk_add_f32 v[126:127], v[126:127], 1.0 op_sel_hi:[1,0]
	v_pk_mul_f32 v[128:129], v[124:125], s[26:27] op_sel_hi:[1,0]
	v_pk_add_f32 v[176:177], v[176:177], 1.0 op_sel_hi:[1,0]
	v_rcp_f32_e32 v126, v126
	v_rcp_f32_e32 v127, v127
	v_exp_f32_e32 v128, v128
	v_exp_f32_e32 v129, v129
	v_rcp_f32_e32 v176, v176
	v_rcp_f32_e32 v177, v177
	v_med3_f32 v110, v110, s63, v167
	v_med3_f32 v111, v111, s63, v167
	v_pk_fma_f32 v[110:111], v[122:123], v[110:111], v[122:123]
	v_pk_add_f32 v[104:105], v[104:105], v[144:145]
	v_pk_mul_f32 v[122:123], v[110:111], v[126:127]
	v_pk_add_f32 v[110:111], v[128:129], 1.0 op_sel_hi:[1,0]
	v_pk_mul_f32 v[118:119], v[118:119], v[176:177]
	v_rcp_f32_e32 v110, v110
	v_rcp_f32_e32 v111, v111
	v_min_f32_e32 v104, 0x40e00000, v104
	v_min_f32_e32 v105, 0x40e00000, v105
	v_pk_add_f32 v[112:113], v[112:113], v[132:133]
	v_cvt_pk_bf16_f32 v118, v118, v119
	v_cvt_pk_bf16_f32 v119, v120, v121
	v_cvt_pk_bf16_f32 v120, v122, v123
	v_pk_mul_f32 v[122:123], v[104:105], s[26:27] op_sel_hi:[1,0]
	v_lshl_or_b32 v172, s36, 7, v170
	v_ashrrev_i32_e32 v155, 31, v154
	v_med3_f32 v112, v112, s63, v167
	v_med3_f32 v113, v113, s63, v167
	v_exp_f32_e32 v122, v122
	v_exp_f32_e32 v123, v123
	v_ashrrev_i32_e32 v173, 31, v172
	v_lshlrev_b64 v[174:175], 12, v[154:155]
	v_pk_fma_f32 v[112:113], v[124:125], v[112:113], v[124:125]
	v_lshl_add_u64 v[174:175], s[12:13], 0, v[174:175]
	v_pk_mul_f32 v[124:125], v[112:113], v[110:111]
	v_lshlrev_b64 v[112:113], 1, v[172:173]
	v_pk_add_f32 v[102:103], v[102:103], v[142:143]
	v_pk_add_f32 v[86:87], v[86:87], v[138:139]
	v_lshl_add_u64 v[110:111], v[174:175], 0, v[112:113]
	v_cvt_pk_bf16_f32 v121, v124, v125
	v_min_f32_e32 v102, 0x40e00000, v102
	v_min_f32_e32 v103, 0x40e00000, v103
	v_med3_f32 v86, v86, s63, v167
	v_med3_f32 v87, v87, s63, v167
	global_store_dwordx4 v[110:111], v[118:121], off
	v_pk_fma_f32 v[86:87], v[102:103], v[86:87], v[102:103]
	v_pk_add_f32 v[88:89], v[88:89], v[140:141]
	v_pk_mul_f32 v[120:121], v[102:103], s[26:27] op_sel_hi:[1,0]
	v_pk_add_f32 v[102:103], v[122:123], 1.0 op_sel_hi:[1,0]
	v_med3_f32 v88, v88, s63, v167
	v_rcp_f32_e32 v102, v102
	v_rcp_f32_e32 v103, v103
	v_med3_f32 v89, v89, s63, v167
	v_pk_add_f32 v[90:91], v[90:91], v[134:135]
	v_pk_fma_f32 v[88:89], v[104:105], v[88:89], v[104:105]
	v_min_f32_e32 v90, 0x40e00000, v90
	v_min_f32_e32 v91, 0x40e00000, v91
	v_pk_mul_f32 v[88:89], v[88:89], v[102:103]
	v_pk_mul_f32 v[102:103], v[90:91], s[26:27] op_sel_hi:[1,0]
	v_pk_add_f32 v[92:93], v[92:93], v[136:137]
	v_exp_f32_e32 v102, v102
	v_exp_f32_e32 v103, v103
	v_min_f32_e32 v92, 0x40e00000, v92
	v_min_f32_e32 v93, 0x40e00000, v93
	v_exp_f32_e32 v120, v120
	v_exp_f32_e32 v121, v121
	v_pk_add_f32 v[102:103], v[102:103], 1.0 op_sel_hi:[1,0]
	v_pk_mul_f32 v[104:105], v[92:93], s[26:27] op_sel_hi:[1,0]
	v_rcp_f32_e32 v102, v102
	v_rcp_f32_e32 v103, v103
	v_exp_f32_e32 v104, v104
	v_exp_f32_e32 v105, v105
	v_pk_add_f32 v[74:75], v[74:75], v[130:131]
	v_pk_add_f32 v[120:121], v[120:121], 1.0 op_sel_hi:[1,0]
	v_med3_f32 v74, v74, s63, v167
	v_med3_f32 v75, v75, s63, v167
	v_pk_fma_f32 v[74:75], v[90:91], v[74:75], v[90:91]
	v_rcp_f32_e32 v120, v120
	v_rcp_f32_e32 v121, v121
	v_pk_mul_f32 v[90:91], v[74:75], v[102:103]
	v_pk_add_f32 v[74:75], v[104:105], 1.0 op_sel_hi:[1,0]
	v_pk_add_f32 v[76:77], v[76:77], v[132:133]
	v_rcp_f32_e32 v74, v74
	v_rcp_f32_e32 v75, v75
	v_med3_f32 v76, v76, s63, v167
	v_med3_f32 v77, v77, s63, v167
	v_pk_add_f32 v[72:73], v[72:73], v[144:145]
	v_pk_mul_f32 v[86:87], v[86:87], v[120:121]
	v_pk_fma_f32 v[76:77], v[92:93], v[76:77], v[92:93]
	v_min_f32_e32 v72, 0x40e00000, v72
	v_min_f32_e32 v73, 0x40e00000, v73
	v_or_b32_e32 v118, 16, v154
	v_pk_mul_f32 v[92:93], v[76:77], v[74:75]
	v_cvt_pk_bf16_f32 v74, v86, v87
	v_pk_mul_f32 v[86:87], v[72:73], s[26:27] op_sel_hi:[1,0]
	v_ashrrev_i32_e32 v119, 31, v118
	v_exp_f32_e32 v86, v86
	v_exp_f32_e32 v87, v87
; __device__ __forceinline__ unsigned cvt_pk_bf16(float lo, float hi) { return cvt2bf(lo, hi); }
;     __device__ __forceinline__ void operator()(const f32x4 (&acc)[2][2][4][2], const Unit& u, int wr, int wc, int fr, int fq, float b1, LAS float* bx) const {
;     ...
;             for (int m = 0; m < 4; ++m) {
;                 bf16* rowp = act + (size_t)(row0 + ai * HALF + m * 16) * DM + col0;
;                 float o[8];
; #pragma unroll
;                 for (int n = 0; n < 2; ++n)
; #pragma unroll
;                     for (int j = 0; j < 4; j += 2) {
;                         const f32x4 gb = n ? g1 : g0, ub = n ? u1 : u0;
;                         const f32x2_t hg = f32x2_t{acc[ai][0][m][n][j], acc[ai][0][m][n][j + 1]} + f32x2_t{gb[j], gb[j + 1]};
;                         const f32x2_t hu = f32x2_t{acc[ai][1][m][n][j], acc[ai][1][m][n][j + 1]} + f32x2_t{ub[j], ub[j + 1]};
;                         const f32x2_t gt = {fminf(hg[0], 7.0f), fminf(hg[1], 7.0f)}, up = {fminf(fmaxf(hu[0], -7.0f), 7.0f), fminf(fmaxf(hu[1], -7.0f), 7.0f)};
;                         const f32x2_t t = gt * (-1.702f * 1.4426950408889634f);
;                         const f32x2_t dn = f32x2_t{__builtin_amdgcn_exp2f(t[0]), __builtin_amdgcn_exp2f(t[1])} + 1.0f;
;                         const f32x2_t sg = {__builtin_amdgcn_rcpf(dn[0]), __builtin_amdgcn_rcpf(dn[1])};
;                         const f32x2_t r2 = (up * gt + gt) * sg;
;                         o[n * 4 + j] = r2[0]; o[n * 4 + j + 1] = r2[1]; }
;                 v4u w; w.x = cvt_pk_bf16(o[0], o[1]); w.y = cvt_pk_bf16(o[2], o[3]); w.z = cvt_pk_bf16(o[4], o[5]); w.w = cvt_pk_bf16(o[6], o[7]);
;                 *(v4u*)rowp = w; }
	v_lshlrev_b64 v[118:119], 12, v[118:119]
	v_lshl_add_u64 v[118:119], s[12:13], 0, v[118:119]
	v_pk_add_f32 v[70:71], v[70:71], v[142:143]
	v_pk_add_f32 v[54:55], v[54:55], v[138:139]
	v_lshl_add_u64 v[102:103], v[118:119], 0, v[112:113]
	v_cvt_pk_bf16_f32 v75, v88, v89
	v_cvt_pk_bf16_f32 v76, v90, v91
	v_cvt_pk_bf16_f32 v77, v92, v93
	v_min_f32_e32 v70, 0x40e00000, v70
	v_min_f32_e32 v71, 0x40e00000, v71
	v_med3_f32 v54, v54, s63, v167
	v_med3_f32 v55, v55, s63, v167
	global_store_dwordx4 v[102:103], v[74:77], off
	v_pk_fma_f32 v[54:55], v[70:71], v[54:55], v[70:71]
	v_pk_add_f32 v[56:57], v[56:57], v[140:141]
	v_pk_mul_f32 v[76:77], v[70:71], s[26:27] op_sel_hi:[1,0]
	v_pk_add_f32 v[70:71], v[86:87], 1.0 op_sel_hi:[1,0]
	v_med3_f32 v56, v56, s63, v167
	v_rcp_f32_e32 v70, v70
	v_rcp_f32_e32 v71, v71
	v_med3_f32 v57, v57, s63, v167
	v_pk_add_f32 v[58:59], v[58:59], v[134:135]
	v_pk_fma_f32 v[56:57], v[72:73], v[56:57], v[72:73]
	v_min_f32_e32 v58, 0x40e00000, v58
	v_min_f32_e32 v59, 0x40e00000, v59
	v_pk_mul_f32 v[56:57], v[56:57], v[70:71]
	v_pk_mul_f32 v[70:71], v[58:59], s[26:27] op_sel_hi:[1,0]
	v_pk_add_f32 v[60:61], v[60:61], v[136:137]
	v_exp_f32_e32 v70, v70
	v_exp_f32_e32 v71, v71
	v_min_f32_e32 v60, 0x40e00000, v60
	v_min_f32_e32 v61, 0x40e00000, v61
	v_exp_f32_e32 v76, v76
	v_exp_f32_e32 v77, v77
	v_pk_add_f32 v[70:71], v[70:71], 1.0 op_sel_hi:[1,0]
	v_pk_mul_f32 v[72:73], v[60:61], s[26:27] op_sel_hi:[1,0]
	v_rcp_f32_e32 v70, v70
	v_rcp_f32_e32 v71, v71
	v_exp_f32_e32 v72, v72
	v_exp_f32_e32 v73, v73
	v_pk_add_f32 v[42:43], v[42:43], v[130:131]
	v_pk_add_f32 v[76:77], v[76:77], 1.0 op_sel_hi:[1,0]
	v_med3_f32 v42, v42, s63, v167
	v_med3_f32 v43, v43, s63, v167
	v_pk_fma_f32 v[42:43], v[58:59], v[42:43], v[58:59]
	v_rcp_f32_e32 v76, v76
	v_rcp_f32_e32 v77, v77
	v_pk_mul_f32 v[58:59], v[42:43], v[70:71]
	v_pk_add_f32 v[42:43], v[72:73], 1.0 op_sel_hi:[1,0]
	v_pk_add_f32 v[44:45], v[44:45], v[132:133]
	v_rcp_f32_e32 v42, v42
	v_rcp_f32_e32 v43, v43
	v_med3_f32 v44, v44, s63, v167
	v_med3_f32 v45, v45, s63, v167
	v_pk_add_f32 v[40:41], v[40:41], v[144:145]
	v_pk_mul_f32 v[54:55], v[54:55], v[76:77]
	v_pk_fma_f32 v[44:45], v[60:61], v[44:45], v[60:61]
	v_min_f32_e32 v40, 0x40e00000, v40
	v_min_f32_e32 v41, 0x40e00000, v41
	v_or_b32_e32 v74, 32, v154
	v_pk_mul_f32 v[60:61], v[44:45], v[42:43]
	v_cvt_pk_bf16_f32 v42, v54, v55
	v_pk_mul_f32 v[54:55], v[40:41], s[26:27] op_sel_hi:[1,0]
	v_ashrrev_i32_e32 v75, 31, v74
	v_exp_f32_e32 v54, v54
	v_exp_f32_e32 v55, v55
	v_lshlrev_b64 v[74:75], 12, v[74:75]
	v_lshl_add_u64 v[74:75], s[12:13], 0, v[74:75]
	v_pk_add_f32 v[38:39], v[38:39], v[142:143]
	v_pk_add_f32 v[22:23], v[22:23], v[138:139]
	v_lshl_add_u64 v[70:71], v[74:75], 0, v[112:113]
	v_cvt_pk_bf16_f32 v43, v56, v57
	v_cvt_pk_bf16_f32 v44, v58, v59
	v_cvt_pk_bf16_f32 v45, v60, v61
	v_min_f32_e32 v38, 0x40e00000, v38
	v_min_f32_e32 v39, 0x40e00000, v39
	v_med3_f32 v22, v22, s63, v167
	v_med3_f32 v23, v23, s63, v167
	global_store_dwordx4 v[70:71], v[42:45], off
	v_pk_fma_f32 v[22:23], v[38:39], v[22:23], v[38:39]
	v_pk_add_f32 v[24:25], v[24:25], v[140:141]
	v_pk_mul_f32 v[44:45], v[38:39], s[26:27] op_sel_hi:[1,0]
	v_pk_add_f32 v[38:39], v[54:55], 1.0 op_sel_hi:[1,0]
	v_med3_f32 v24, v24, s63, v167
	v_rcp_f32_e32 v38, v38
	v_rcp_f32_e32 v39, v39
	v_med3_f32 v25, v25, s63, v167
	v_pk_add_f32 v[26:27], v[26:27], v[134:135]
	v_pk_fma_f32 v[24:25], v[40:41], v[24:25], v[40:41]
	v_min_f32_e32 v26, 0x40e00000, v26
	v_min_f32_e32 v27, 0x40e00000, v27
	v_pk_mul_f32 v[24:25], v[24:25], v[38:39]
	v_pk_mul_f32 v[38:39], v[26:27], s[26:27] op_sel_hi:[1,0]
	v_pk_add_f32 v[28:29], v[28:29], v[136:137]
	v_exp_f32_e32 v38, v38
	v_exp_f32_e32 v39, v39
	v_min_f32_e32 v28, 0x40e00000, v28
	v_min_f32_e32 v29, 0x40e00000, v29
	v_pk_mul_f32 v[40:41], v[28:29], s[26:27] op_sel_hi:[1,0]
	v_pk_add_f32 v[38:39], v[38:39], 1.0 op_sel_hi:[1,0]
	v_exp_f32_e32 v44, v44
	v_exp_f32_e32 v45, v45
	v_rcp_f32_e32 v38, v38
	v_rcp_f32_e32 v39, v39
	v_exp_f32_e32 v40, v40
	v_exp_f32_e32 v41, v41
	v_pk_add_f32 v[10:11], v[10:11], v[130:131]
	v_pk_add_f32 v[44:45], v[44:45], 1.0 op_sel_hi:[1,0]
	v_med3_f32 v10, v10, s63, v167
	v_med3_f32 v11, v11, s63, v167
	v_pk_fma_f32 v[10:11], v[26:27], v[10:11], v[26:27]
	v_rcp_f32_e32 v44, v44
	v_pk_mul_f32 v[26:27], v[10:11], v[38:39]
	v_pk_add_f32 v[10:11], v[40:41], 1.0 op_sel_hi:[1,0]
	v_rcp_f32_e32 v45, v45
	v_rcp_f32_e32 v10, v10
	v_rcp_f32_e32 v11, v11
	v_or_b32_e32 v42, 48, v154
	v_pk_add_f32 v[12:13], v[12:13], v[132:133]
	v_ashrrev_i32_e32 v43, 31, v42
	v_med3_f32 v12, v12, s63, v167
	v_med3_f32 v13, v13, s63, v167
	v_lshlrev_b64 v[42:43], 12, v[42:43]
	v_pk_fma_f32 v[12:13], v[28:29], v[12:13], v[28:29]
	v_lshl_add_u64 v[42:43], s[12:13], 0, v[42:43]
	v_pk_mul_f32 v[22:23], v[22:23], v[44:45]
	v_pk_mul_f32 v[28:29], v[12:13], v[10:11]
	v_lshl_add_u64 v[38:39], v[42:43], 0, v[112:113]
	v_cvt_pk_bf16_f32 v10, v22, v23
	v_cvt_pk_bf16_f32 v11, v24, v25
	v_cvt_pk_bf16_f32 v12, v26, v27
	v_cvt_pk_bf16_f32 v13, v28, v29
	global_store_dwordx4 v[38:39], v[10:13], off
	v_pk_add_f32 v[26:27], v[106:107], v[138:139]
	v_pk_add_f32 v[24:25], v[108:109], v[140:141]
	v_pk_add_f32 v[12:13], v[114:115], v[142:143]
	v_pk_add_f32 v[10:11], v[116:117], v[144:145]
	v_min_f32_e32 v12, 0x40e00000, v12
	v_min_f32_e32 v13, 0x40e00000, v13
	v_pk_mul_f32 v[22:23], v[12:13], s[26:27] op_sel_hi:[1,0]
	v_min_f32_e32 v10, 0x40e00000, v10
	v_exp_f32_e32 v22, v22
	v_exp_f32_e32 v23, v23
	v_min_f32_e32 v11, 0x40e00000, v11
	v_pk_mul_f32 v[28:29], v[10:11], s[26:27] op_sel_hi:[1,0]
	v_med3_f32 v26, v26, s63, v167
	v_pk_add_f32 v[22:23], v[22:23], 1.0 op_sel_hi:[1,0]
; __device__ __forceinline__ unsigned cvt_pk_bf16(float lo, float hi) { return cvt2bf(lo, hi); }
;     __device__ __forceinline__ void operator()(const f32x4 (&acc)[2][2][4][2], const Unit& u, int wr, int wc, int fr, int fq, float b1, LAS float* bx) const {
;     ...
;         for (int ai = 0; ai < 2; ++ai)
; #pragma unroll
;             for (int m = 0; m < 4; ++m) {
;                 bf16* rowp = act + (size_t)(row0 + ai * HALF + m * 16) * DM + col0;
;                 float o[8];
; #pragma unroll
;                 for (int n = 0; n < 2; ++n)
; #pragma unroll
;                     for (int j = 0; j < 4; j += 2) {
;                         const f32x4 gb = n ? g1 : g0, ub = n ? u1 : u0;
;                         const f32x2_t hg = f32x2_t{acc[ai][0][m][n][j], acc[ai][0][m][n][j + 1]} + f32x2_t{gb[j], gb[j + 1]};
;                         const f32x2_t hu = f32x2_t{acc[ai][1][m][n][j], acc[ai][1][m][n][j + 1]} + f32x2_t{ub[j], ub[j + 1]};
;                         const f32x2_t gt = {fminf(hg[0], 7.0f), fminf(hg[1], 7.0f)}, up = {fminf(fmaxf(hu[0], -7.0f), 7.0f), fminf(fmaxf(hu[1], -7.0f), 7.0f)};
;                         const f32x2_t t = gt * (-1.702f * 1.4426950408889634f);
;                         const f32x2_t dn = f32x2_t{__builtin_amdgcn_exp2f(t[0]), __builtin_amdgcn_exp2f(t[1])} + 1.0f;
;                         const f32x2_t sg = {__builtin_amdgcn_rcpf(dn[0]), __builtin_amdgcn_rcpf(dn[1])};
;                         const f32x2_t r2 = (up * gt + gt) * sg;
;                         o[n * 4 + j] = r2[0]; o[n * 4 + j + 1] = r2[1]; }
;                 v4u w; w.x = cvt_pk_bf16(o[0], o[1]); w.y = cvt_pk_bf16(o[2], o[3]); w.z = cvt_pk_bf16(o[4], o[5]); w.w = cvt_pk_bf16(o[6], o[7]);
;                 *(v4u*)rowp = w; }
	v_exp_f32_e32 v28, v28
	v_rcp_f32_e32 v22, v22
	v_rcp_f32_e32 v23, v23
	v_exp_f32_e32 v29, v29
	v_med3_f32 v27, v27, s63, v167
	v_pk_fma_f32 v[12:13], v[12:13], v[26:27], v[12:13]
	v_med3_f32 v24, v24, s63, v167
	v_med3_f32 v25, v25, s63, v167
	v_pk_mul_f32 v[12:13], v[12:13], v[22:23]
	v_pk_add_f32 v[22:23], v[28:29], 1.0 op_sel_hi:[1,0]
	v_pk_fma_f32 v[10:11], v[10:11], v[24:25], v[10:11]
	v_pk_add_f32 v[24:25], v[98:99], v[134:135]
	v_rcp_f32_e32 v22, v22
	v_rcp_f32_e32 v23, v23
	v_min_f32_e32 v24, 0x40e00000, v24
	v_min_f32_e32 v25, 0x40e00000, v25
	v_pk_mul_f32 v[26:27], v[24:25], s[26:27] op_sel_hi:[1,0]
	v_pk_mul_f32 v[22:23], v[10:11], v[22:23]
	v_exp_f32_e32 v26, v26
	v_exp_f32_e32 v27, v27
	v_pk_add_f32 v[10:11], v[100:101], v[136:137]
	v_pk_add_f32 v[38:39], v[94:95], v[130:131]
	v_min_f32_e32 v10, 0x40e00000, v10
	v_min_f32_e32 v11, 0x40e00000, v11
	v_pk_add_f32 v[26:27], v[26:27], 1.0 op_sel_hi:[1,0]
	v_pk_mul_f32 v[40:41], v[10:11], s[26:27] op_sel_hi:[1,0]
	v_rcp_f32_e32 v26, v26
	v_rcp_f32_e32 v27, v27
	v_exp_f32_e32 v40, v40
	v_exp_f32_e32 v41, v41
	v_med3_f32 v38, v38, s63, v167
	v_med3_f32 v39, v39, s63, v167
	v_pk_fma_f32 v[24:25], v[24:25], v[38:39], v[24:25]
	v_pk_add_f32 v[28:29], v[96:97], v[132:133]
	v_pk_mul_f32 v[24:25], v[24:25], v[26:27]
	v_pk_add_f32 v[26:27], v[40:41], 1.0 op_sel_hi:[1,0]
	v_med3_f32 v28, v28, s63, v167
	v_rcp_f32_e32 v26, v26
	v_rcp_f32_e32 v27, v27
	v_med3_f32 v29, v29, s63, v167
	v_pk_fma_f32 v[10:11], v[10:11], v[28:29], v[10:11]
	s_mov_b32 s5, 0x80000
	v_pk_mul_f32 v[26:27], v[10:11], v[26:27]
	v_cvt_pk_bf16_f32 v11, v22, v23
	v_add_co_u32_e32 v22, vcc, s5, v110
	v_cvt_pk_bf16_f32 v10, v12, v13
	v_cvt_pk_bf16_f32 v12, v24, v25
	v_cvt_pk_bf16_f32 v13, v26, v27
	v_addc_co_u32_e32 v23, vcc, 0, v111, vcc
	global_store_dwordx4 v[22:23], v[10:13], off
	v_pk_add_f32 v[26:27], v[78:79], v[138:139]
	v_pk_add_f32 v[24:25], v[80:81], v[140:141]
	v_pk_add_f32 v[12:13], v[82:83], v[142:143]
	v_pk_add_f32 v[10:11], v[84:85], v[144:145]
	v_min_f32_e32 v12, 0x40e00000, v12
	v_min_f32_e32 v13, 0x40e00000, v13
	v_pk_mul_f32 v[22:23], v[12:13], s[26:27] op_sel_hi:[1,0]
	v_min_f32_e32 v10, 0x40e00000, v10
	v_exp_f32_e32 v22, v22
	v_exp_f32_e32 v23, v23
	v_min_f32_e32 v11, 0x40e00000, v11
	v_pk_mul_f32 v[28:29], v[10:11], s[26:27] op_sel_hi:[1,0]
	v_med3_f32 v26, v26, s63, v167
	v_pk_add_f32 v[22:23], v[22:23], 1.0 op_sel_hi:[1,0]
	v_exp_f32_e32 v28, v28
	v_rcp_f32_e32 v22, v22
	v_rcp_f32_e32 v23, v23
	v_exp_f32_e32 v29, v29
	v_med3_f32 v27, v27, s63, v167
	v_pk_fma_f32 v[12:13], v[12:13], v[26:27], v[12:13]
	v_med3_f32 v24, v24, s63, v167
	v_med3_f32 v25, v25, s63, v167
	v_pk_mul_f32 v[12:13], v[12:13], v[22:23]
	v_pk_add_f32 v[22:23], v[28:29], 1.0 op_sel_hi:[1,0]
	v_pk_fma_f32 v[10:11], v[10:11], v[24:25], v[10:11]
	v_pk_add_f32 v[24:25], v[66:67], v[134:135]
	v_rcp_f32_e32 v22, v22
	v_rcp_f32_e32 v23, v23
	v_min_f32_e32 v24, 0x40e00000, v24
	v_min_f32_e32 v25, 0x40e00000, v25
	v_pk_mul_f32 v[26:27], v[24:25], s[26:27] op_sel_hi:[1,0]
	v_pk_mul_f32 v[22:23], v[10:11], v[22:23]
	v_exp_f32_e32 v26, v26
	v_exp_f32_e32 v27, v27
	v_pk_add_f32 v[10:11], v[68:69], v[136:137]
	v_pk_add_f32 v[38:39], v[62:63], v[130:131]
	v_min_f32_e32 v10, 0x40e00000, v10
	v_min_f32_e32 v11, 0x40e00000, v11
	v_pk_add_f32 v[26:27], v[26:27], 1.0 op_sel_hi:[1,0]
	v_pk_mul_f32 v[40:41], v[10:11], s[26:27] op_sel_hi:[1,0]
	v_rcp_f32_e32 v26, v26
	v_rcp_f32_e32 v27, v27
	v_exp_f32_e32 v40, v40
	v_exp_f32_e32 v41, v41
	v_med3_f32 v38, v38, s63, v167
	v_med3_f32 v39, v39, s63, v167
	v_pk_fma_f32 v[24:25], v[24:25], v[38:39], v[24:25]
	v_pk_add_f32 v[28:29], v[64:65], v[132:133]
	v_pk_mul_f32 v[24:25], v[24:25], v[26:27]
	v_pk_add_f32 v[26:27], v[40:41], 1.0 op_sel_hi:[1,0]
	v_med3_f32 v28, v28, s63, v167
	v_rcp_f32_e32 v26, v26
	v_rcp_f32_e32 v27, v27
	v_med3_f32 v29, v29, s63, v167
	v_pk_fma_f32 v[10:11], v[10:11], v[28:29], v[10:11]
	s_mov_b32 s5, 0x90000
	v_pk_mul_f32 v[26:27], v[10:11], v[26:27]
	v_cvt_pk_bf16_f32 v11, v22, v23
	v_add_co_u32_e32 v22, vcc, s5, v110
	v_cvt_pk_bf16_f32 v10, v12, v13
	v_cvt_pk_bf16_f32 v12, v24, v25
	v_cvt_pk_bf16_f32 v13, v26, v27
	v_addc_co_u32_e32 v23, vcc, 0, v111, vcc
	global_store_dwordx4 v[22:23], v[10:13], off
	v_pk_add_f32 v[26:27], v[46:47], v[138:139]
	v_pk_add_f32 v[24:25], v[48:49], v[140:141]
	v_pk_add_f32 v[12:13], v[50:51], v[142:143]
	v_pk_add_f32 v[10:11], v[52:53], v[144:145]
	v_min_f32_e32 v12, 0x40e00000, v12
	v_min_f32_e32 v13, 0x40e00000, v13
	v_pk_mul_f32 v[22:23], v[12:13], s[26:27] op_sel_hi:[1,0]
	v_min_f32_e32 v10, 0x40e00000, v10
	v_exp_f32_e32 v22, v22
	v_exp_f32_e32 v23, v23
	v_min_f32_e32 v11, 0x40e00000, v11
	v_pk_mul_f32 v[28:29], v[10:11], s[26:27] op_sel_hi:[1,0]
	v_med3_f32 v26, v26, s63, v167
	v_pk_add_f32 v[22:23], v[22:23], 1.0 op_sel_hi:[1,0]
	v_exp_f32_e32 v28, v28
	v_rcp_f32_e32 v22, v22
	v_rcp_f32_e32 v23, v23
	v_exp_f32_e32 v29, v29
	v_med3_f32 v27, v27, s63, v167
	v_pk_fma_f32 v[12:13], v[12:13], v[26:27], v[12:13]
; __device__ __forceinline__ unsigned cvt_pk_bf16(float lo, float hi) { return cvt2bf(lo, hi); }
; template <class Epi, class Sched>
; __device__ __forceinline__ void gemm_phase(LAS unsigned char* lds, const Sched& S, const Epi& E) {
;     ...
;         cur = nxt; cA = nA; cB = nB; ++ui;
;         b1 = E.pre(cur, wc, lane);
;         if constexpr (Sched::GATHER) { PG8_GIDX(vg, cur); }
;     __device__ __forceinline__ void operator()(const f32x4 (&acc)[2][2][4][2], const Unit& u, int wr, int wc, int fr, int fq, float b1, LAS float* bx) const {
;     ...
;         for (int ai = 0; ai < 2; ++ai)
; #pragma unroll
;             for (int m = 0; m < 4; ++m) {
;                 bf16* rowp = act + (size_t)(row0 + ai * HALF + m * 16) * DM + col0;
;                 float o[8];
; #pragma unroll
;                 for (int n = 0; n < 2; ++n)
; #pragma unroll
;                     for (int j = 0; j < 4; j += 2) {
;                         const f32x4 gb = n ? g1 : g0, ub = n ? u1 : u0;
;                         const f32x2_t hg = f32x2_t{acc[ai][0][m][n][j], acc[ai][0][m][n][j + 1]} + f32x2_t{gb[j], gb[j + 1]};
;                         const f32x2_t hu = f32x2_t{acc[ai][1][m][n][j], acc[ai][1][m][n][j + 1]} + f32x2_t{ub[j], ub[j + 1]};
;                         const f32x2_t gt = {fminf(hg[0], 7.0f), fminf(hg[1], 7.0f)}, up = {fminf(fmaxf(hu[0], -7.0f), 7.0f), fminf(fmaxf(hu[1], -7.0f), 7.0f)};
;                         const f32x2_t t = gt * (-1.702f * 1.4426950408889634f);
;                         const f32x2_t dn = f32x2_t{__builtin_amdgcn_exp2f(t[0]), __builtin_amdgcn_exp2f(t[1])} + 1.0f;
;                         const f32x2_t sg = {__builtin_amdgcn_rcpf(dn[0]), __builtin_amdgcn_rcpf(dn[1])};
;                         const f32x2_t r2 = (up * gt + gt) * sg;
;                         o[n * 4 + j] = r2[0]; o[n * 4 + j + 1] = r2[1]; }
;                 v4u w; w.x = cvt_pk_bf16(o[0], o[1]); w.y = cvt_pk_bf16(o[2], o[3]); w.z = cvt_pk_bf16(o[4], o[5]); w.w = cvt_pk_bf16(o[6], o[7]);
;                 *(v4u*)rowp = w; }
	v_med3_f32 v24, v24, s63, v167
	v_med3_f32 v25, v25, s63, v167
	v_pk_mul_f32 v[12:13], v[12:13], v[22:23]
	v_pk_add_f32 v[22:23], v[28:29], 1.0 op_sel_hi:[1,0]
	v_pk_fma_f32 v[10:11], v[10:11], v[24:25], v[10:11]
	v_pk_add_f32 v[24:25], v[34:35], v[134:135]
	v_rcp_f32_e32 v22, v22
	v_rcp_f32_e32 v23, v23
	v_min_f32_e32 v24, 0x40e00000, v24
	v_min_f32_e32 v25, 0x40e00000, v25
	v_pk_mul_f32 v[26:27], v[24:25], s[26:27] op_sel_hi:[1,0]
	v_pk_mul_f32 v[22:23], v[10:11], v[22:23]
	v_exp_f32_e32 v26, v26
	v_exp_f32_e32 v27, v27
	v_pk_add_f32 v[10:11], v[36:37], v[136:137]
	v_pk_add_f32 v[28:29], v[32:33], v[132:133]
	v_min_f32_e32 v10, 0x40e00000, v10
	v_min_f32_e32 v11, 0x40e00000, v11
	v_pk_add_f32 v[26:27], v[26:27], 1.0 op_sel_hi:[1,0]
	v_pk_mul_f32 v[32:33], v[10:11], s[26:27] op_sel_hi:[1,0]
	v_rcp_f32_e32 v26, v26
	v_rcp_f32_e32 v27, v27
	v_exp_f32_e32 v32, v32
	v_exp_f32_e32 v33, v33
	v_pk_add_f32 v[30:31], v[30:31], v[130:131]
	v_med3_f32 v28, v28, s63, v167
	v_med3_f32 v30, v30, s63, v167
	v_med3_f32 v31, v31, s63, v167
	v_pk_fma_f32 v[24:25], v[24:25], v[30:31], v[24:25]
	v_med3_f32 v29, v29, s63, v167
	v_pk_mul_f32 v[24:25], v[24:25], v[26:27]
	v_pk_add_f32 v[26:27], v[32:33], 1.0 op_sel_hi:[1,0]
	v_pk_fma_f32 v[10:11], v[10:11], v[28:29], v[10:11]
	v_rcp_f32_e32 v26, v26
	v_rcp_f32_e32 v27, v27
	s_mov_b32 s5, 0xa0000
	v_pk_add_f32 v[14:15], v[14:15], v[138:139]
	v_pk_add_f32 v[16:17], v[16:17], v[140:141]
	v_pk_mul_f32 v[26:27], v[10:11], v[26:27]
	v_cvt_pk_bf16_f32 v11, v22, v23
	v_add_co_u32_e32 v22, vcc, s5, v110
	v_cvt_pk_bf16_f32 v10, v12, v13
	v_cvt_pk_bf16_f32 v12, v24, v25
	v_cvt_pk_bf16_f32 v13, v26, v27
	v_addc_co_u32_e32 v23, vcc, 0, v111, vcc
	global_store_dwordx4 v[22:23], v[10:13], off
	v_med3_f32 v14, v14, s63, v167
	v_med3_f32 v15, v15, s63, v167
	v_pk_add_f32 v[10:11], v[20:21], v[144:145]
	v_pk_add_f32 v[12:13], v[18:19], v[142:143]
	v_min_f32_e32 v10, 0x40e00000, v10
	v_min_f32_e32 v11, 0x40e00000, v11
	v_pk_mul_f32 v[20:21], v[10:11], s[26:27] op_sel_hi:[1,0]
	v_min_f32_e32 v12, 0x40e00000, v12
	v_exp_f32_e32 v20, v20
	v_exp_f32_e32 v21, v21
	v_min_f32_e32 v13, 0x40e00000, v13
	v_pk_mul_f32 v[18:19], v[12:13], s[26:27] op_sel_hi:[1,0]
	v_pk_fma_f32 v[12:13], v[12:13], v[14:15], v[12:13]
	v_pk_add_f32 v[14:15], v[20:21], 1.0 op_sel_hi:[1,0]
	v_med3_f32 v16, v16, s63, v167
	v_rcp_f32_e32 v14, v14
	v_rcp_f32_e32 v15, v15
	v_med3_f32 v17, v17, s63, v167
	v_pk_add_f32 v[6:7], v[6:7], v[134:135]
	v_pk_fma_f32 v[10:11], v[10:11], v[16:17], v[10:11]
	v_min_f32_e32 v6, 0x40e00000, v6
	v_min_f32_e32 v7, 0x40e00000, v7
	v_pk_mul_f32 v[10:11], v[10:11], v[14:15]
	v_pk_mul_f32 v[14:15], v[6:7], s[26:27] op_sel_hi:[1,0]
	v_pk_add_f32 v[8:9], v[8:9], v[136:137]
	v_exp_f32_e32 v14, v14
	v_exp_f32_e32 v15, v15
	v_min_f32_e32 v8, 0x40e00000, v8
	v_min_f32_e32 v9, 0x40e00000, v9
	v_pk_mul_f32 v[16:17], v[8:9], s[26:27] op_sel_hi:[1,0]
	v_pk_add_f32 v[14:15], v[14:15], 1.0 op_sel_hi:[1,0]
	v_exp_f32_e32 v16, v16
	v_rcp_f32_e32 v14, v14
	v_rcp_f32_e32 v15, v15
	v_exp_f32_e32 v17, v17
	v_exp_f32_e32 v18, v18
	v_exp_f32_e32 v19, v19
	v_pk_add_f32 v[2:3], v[2:3], v[130:131]
	v_pk_add_f32 v[4:5], v[4:5], v[132:133]
	v_med3_f32 v2, v2, s63, v167
	v_med3_f32 v3, v3, s63, v167
	v_pk_fma_f32 v[2:3], v[6:7], v[2:3], v[6:7]
	v_pk_add_f32 v[18:19], v[18:19], 1.0 op_sel_hi:[1,0]
	v_pk_mul_f32 v[6:7], v[2:3], v[14:15]
	v_pk_add_f32 v[2:3], v[16:17], 1.0 op_sel_hi:[1,0]
	v_rcp_f32_e32 v18, v18
	v_rcp_f32_e32 v2, v2
	v_rcp_f32_e32 v3, v3
	v_rcp_f32_e32 v19, v19
	v_med3_f32 v4, v4, s63, v167
	v_med3_f32 v5, v5, s63, v167
	v_pk_fma_f32 v[4:5], v[8:9], v[4:5], v[8:9]
	v_pk_mul_f32 v[12:13], v[12:13], v[18:19]
	v_pk_mul_f32 v[8:9], v[4:5], v[2:3]
	v_cvt_pk_bf16_f32 v4, v6, v7
	v_add_co_u32_e32 v6, vcc, 0xb0000, v110
	v_cvt_pk_bf16_f32 v2, v12, v13
	s_nop 0
	v_addc_co_u32_e32 v7, vcc, 0, v111, vcc
	v_cvt_pk_bf16_f32 v3, v10, v11
	v_cvt_pk_bf16_f32 v5, v8, v9
	s_andn2_b64 vcc, exec, s[34:35]
	s_mov_b64 s[18:19], -1
	global_store_dwordx4 v[6:7], v[2:5], off
	s_cbranch_vccnz .LBB0_1250
	s_ashr_i32 s29, s28, 31
	s_lshl_b32 s14, s4, 7
	s_ashr_i32 s15, s14, 31
	s_lshl_b64 s[18:19], s[28:29], 14
	s_add_u32 s5, s50, s18
	s_addc_u32 s18, s51, s19
	s_lshl_b64 s[14:15], s[14:15], 2
	s_add_u32 s5, s5, s14
	s_addc_u32 s15, s18, s15
	s_add_u32 s14, s5, s37
	s_addc_u32 s15, s15, 0
	v_lshl_add_u64 v[2:3], s[14:15], 0, v[148:149]
	v_mov_b32_e32 v153, v149
	v_lshl_add_u64 v[2:3], v[2:3], 0, v[152:153]
	global_load_dword v130, v[2:3], off
	s_sub_i32 s5, s82, s54
	v_med3_i32 v2, s5, 0, 47
	v_lshl_add_u32 v2, v2, 9, v163
	v_lshl_add_u32 v3, v164, 1, v2
	v_lshl_add_u32 v2, v165, 1, v2
	ds_read_u16 v4, v3
	ds_read_u16 v3, v3 offset:256
	ds_read_u16 v5, v2
	ds_read_u16 v2, v2 offset:256
	s_mov_b64 s[18:19], 0
	s_waitcnt lgkmcnt(3)
	v_lshl_or_b32 v131, v4, 12, v147
	s_waitcnt lgkmcnt(2)
	v_lshl_or_b32 v132, v3, 12, v147
	s_waitcnt lgkmcnt(1)
	v_lshl_or_b32 v133, v5, 12, v147
	s_waitcnt lgkmcnt(0)
	v_lshl_or_b32 v134, v2, 12, v147

; #define LAS __attribute__((address_space(3)))
; __device__ __forceinline__ unsigned cvt_pk_bf16(float lo, float hi) { return cvt2bf(lo, hi); }
;     __device__ __forceinline__ void operator()(const f32x4 (&acc)[2][2][4][2], const Unit& u, int wr, int wc, int fr, int fq, float b1, LAS float* bx) const {
;         const int row0 = u.pm * BM + wr * 64 + fr, col0 = u.pn * BM + wc * 32 + 8 * fq;
;         bx[threadIdx.x & 63] = b1;
;         f32x4 bv[2][2];
; #pragma unroll
;         for (int bj = 0; bj < 2; ++bj)
; #pragma unroll
;             for (int n = 0; n < 2; ++n) bv[bj][n] = *(const LAS f32x4*)(bx + bj * 32 + 8 * fq + 4 * n);
; #pragma unroll
;         for (int ai = 0; ai < 2; ++ai)
; #pragma unroll
;             for (int m = 0; m < 4; ++m) { bf16* rowp = ys + (size_t)(row0 + ai * HALF + m * 16) * DM + col0;
; #pragma unroll
;                 for (int bj = 0; bj < 2; ++bj) { const f32x4 v0 = acc[ai][bj][m][0] + bv[bj][0], v1 = acc[ai][bj][m][1] + bv[bj][1];
;                     v4u w; w.x = cvt_pk_bf16(v0[0], v0[1]); w.y = cvt_pk_bf16(v0[2], v0[3]); w.z = cvt_pk_bf16(v1[0], v1[1]); w.w = cvt_pk_bf16(v1[2], v1[3]);
;                     *(v4u*)(rowp + bj * HALF) = w; } }
.LBB0_1463:
	v_lshl_add_u32 v164, s42, 8, v155
	s_waitcnt vmcnt(8)
	ds_write_b32 v156, v130
	ds_read_b128 v[142:145], v157
	ds_read_b128 v[138:141], v157 offset:16
	ds_read_b128 v[134:137], v157 offset:128
	ds_read_b128 v[130:133], v157 offset:144
	v_lshl_or_b32 v150, s40, 8, v158
	v_ashrrev_i32_e32 v165, 31, v164
	v_ashrrev_i32_e32 v151, 31, v150
	v_lshlrev_b64 v[166:167], 12, v[164:165]
	v_lshl_add_u64 v[166:167], s[14:15], 0, v[166:167]
	v_lshlrev_b64 v[168:169], 1, v[150:151]
	v_lshl_add_u64 v[150:151], v[166:167], 0, v[168:169]
	s_waitcnt lgkmcnt(3)
	v_pk_add_f32 v[64:65], v[64:65], v[144:145]
	v_pk_add_f32 v[62:63], v[62:63], v[142:143]
	s_waitcnt lgkmcnt(2)
	v_pk_add_f32 v[166:167], v[60:61], v[140:141]
	v_pk_add_f32 v[60:61], v[58:59], v[138:139]
	v_cvt_pk_bf16_f32 v58, v62, v63
	v_cvt_pk_bf16_f32 v59, v64, v65
	v_cvt_pk_bf16_f32 v60, v60, v61
	v_cvt_pk_bf16_f32 v61, v166, v167
	global_store_dwordx4 v[150:151], v[58:61], off
	s_waitcnt lgkmcnt(1)
	v_pk_add_f32 v[48:49], v[48:49], v[136:137]
	v_pk_add_f32 v[46:47], v[46:47], v[134:135]
	s_waitcnt lgkmcnt(0)
	v_pk_add_f32 v[58:59], v[44:45], v[132:133]
	v_pk_add_f32 v[44:45], v[42:43], v[130:131]
	v_cvt_pk_bf16_f32 v42, v46, v47
	v_cvt_pk_bf16_f32 v43, v48, v49
	v_cvt_pk_bf16_f32 v44, v44, v45
	v_cvt_pk_bf16_f32 v45, v58, v59
	global_store_dwordx4 v[150:151], v[42:45], off offset:256
	v_pk_add_f32 v[48:49], v[52:53], v[140:141]
	v_pk_add_f32 v[50:51], v[50:51], v[138:139]
	v_or_b32_e32 v42, 16, v164
	v_ashrrev_i32_e32 v43, 31, v42
	v_lshlrev_b64 v[42:43], 12, v[42:43]
	v_lshl_add_u64 v[42:43], s[14:15], 0, v[42:43]
	v_lshl_add_u64 v[46:47], v[42:43], 0, v[168:169]
	v_pk_add_f32 v[44:45], v[56:57], v[144:145]
	v_pk_add_f32 v[42:43], v[54:55], v[142:143]
	v_pk_add_f32 v[32:33], v[32:33], v[136:137]
	v_cvt_pk_bf16_f32 v42, v42, v43
	v_cvt_pk_bf16_f32 v43, v44, v45
	v_cvt_pk_bf16_f32 v44, v50, v51
	v_cvt_pk_bf16_f32 v45, v48, v49
	global_store_dwordx4 v[46:47], v[42:45], off
	v_pk_add_f32 v[30:31], v[30:31], v[134:135]
	v_pk_add_f32 v[34:35], v[34:35], v[138:139]
	v_pk_add_f32 v[42:43], v[28:29], v[132:133]
	v_pk_add_f32 v[28:29], v[26:27], v[130:131]
	v_cvt_pk_bf16_f32 v26, v30, v31
	v_cvt_pk_bf16_f32 v27, v32, v33
	v_cvt_pk_bf16_f32 v28, v28, v29
	v_cvt_pk_bf16_f32 v29, v42, v43
	global_store_dwordx4 v[46:47], v[26:29], off offset:256
	v_pk_add_f32 v[32:33], v[36:37], v[140:141]
	v_pk_add_f32 v[16:17], v[16:17], v[136:137]
	v_or_b32_e32 v26, 32, v164
	v_ashrrev_i32_e32 v27, 31, v26
	v_lshlrev_b64 v[26:27], 12, v[26:27]
	v_lshl_add_u64 v[26:27], s[14:15], 0, v[26:27]
	v_lshl_add_u64 v[30:31], v[26:27], 0, v[168:169]
	v_pk_add_f32 v[28:29], v[40:41], v[144:145]
	v_pk_add_f32 v[26:27], v[38:39], v[142:143]
	v_pk_add_f32 v[14:15], v[14:15], v[134:135]
	v_cvt_pk_bf16_f32 v26, v26, v27
	v_cvt_pk_bf16_f32 v27, v28, v29
	v_cvt_pk_bf16_f32 v28, v34, v35
	v_cvt_pk_bf16_f32 v29, v32, v33
	global_store_dwordx4 v[30:31], v[26:29], off
	v_pk_add_f32 v[18:19], v[18:19], v[138:139]
	v_pk_add_f32 v[8:9], v[8:9], v[136:137]
	v_pk_add_f32 v[26:27], v[12:13], v[132:133]
	v_pk_add_f32 v[12:13], v[10:11], v[130:131]
	v_cvt_pk_bf16_f32 v10, v14, v15
	v_cvt_pk_bf16_f32 v11, v16, v17
	v_cvt_pk_bf16_f32 v12, v12, v13
	v_cvt_pk_bf16_f32 v13, v26, v27
	global_store_dwordx4 v[30:31], v[10:13], off offset:256
	v_pk_add_f32 v[16:17], v[20:21], v[140:141]
	v_pk_add_f32 v[6:7], v[6:7], v[134:135]
	v_or_b32_e32 v10, 48, v164
	v_ashrrev_i32_e32 v11, 31, v10
	v_lshlrev_b64 v[10:11], 12, v[10:11]
	v_lshl_add_u64 v[10:11], s[14:15], 0, v[10:11]
	v_lshl_add_u64 v[14:15], v[10:11], 0, v[168:169]
	v_pk_add_f32 v[12:13], v[24:25], v[144:145]
	v_pk_add_f32 v[10:11], v[22:23], v[142:143]
	s_mov_b64 s[10:11], -1
	v_cvt_pk_bf16_f32 v10, v10, v11
	v_cvt_pk_bf16_f32 v11, v12, v13
	v_cvt_pk_bf16_f32 v12, v18, v19
	v_cvt_pk_bf16_f32 v13, v16, v17
	global_store_dwordx4 v[14:15], v[10:13], off
	s_nop 1
	v_pk_add_f32 v[10:11], v[4:5], v[132:133]
	v_pk_add_f32 v[4:5], v[2:3], v[130:131]
	v_cvt_pk_bf16_f32 v2, v6, v7
	v_cvt_pk_bf16_f32 v3, v8, v9
	v_cvt_pk_bf16_f32 v4, v4, v5
	v_cvt_pk_bf16_f32 v5, v10, v11
	global_store_dwordx4 v[14:15], v[2:5], off offset:256
; __device__ __forceinline__ unsigned cvt_pk_bf16(float lo, float hi) { return cvt2bf(lo, hi); }
; #define PG8_BAR __builtin_amdgcn_s_barrier()
; template <class Epi, class Sched>
; __device__ __forceinline__ void gemm_phase(LAS unsigned char* lds, const Sched& S, const Epi& E) {
;     ...
;         cur = nxt; cA = nA; cB = nB; ++ui;
;         b1 = E.pre(cur, wc, lane);
;         if constexpr (Sched::GATHER) { PG8_GIDX(vg, cur); }
;         if constexpr (Epi::ALIGN) { if (wr == 1) PG8_BAR; }
;     __device__ __forceinline__ void operator()(const f32x4 (&acc)[2][2][4][2], const Unit& u, int wr, int wc, int fr, int fq, float b1, LAS float* bx) const {
;     ...
;         for (int ai = 0; ai < 2; ++ai)
; #pragma unroll
;             for (int m = 0; m < 4; ++m) { bf16* rowp = ys + (size_t)(row0 + ai * HALF + m * 16) * DM + col0;
; #pragma unroll
;                 for (int bj = 0; bj < 2; ++bj) { const f32x4 v0 = acc[ai][bj][m][0] + bv[bj][0], v1 = acc[ai][bj][m][1] + bv[bj][1];
;                     v4u w; w.x = cvt_pk_bf16(v0[0], v0[1]); w.y = cvt_pk_bf16(v0[2], v0[3]); w.z = cvt_pk_bf16(v1[0], v1[1]); w.w = cvt_pk_bf16(v1[2], v1[3]);
;                     *(v4u*)(rowp + bj * HALF) = w; } }
	v_pk_add_f32 v[8:9], v[124:125], v[140:141]
	v_pk_add_f32 v[10:11], v[122:123], v[138:139]
	v_pk_add_f32 v[4:5], v[128:129], v[144:145]
	v_pk_add_f32 v[2:3], v[126:127], v[142:143]
	v_lshl_add_u64 v[6:7], v[150:151], 0, s[18:19]
	v_cvt_pk_bf16_f32 v2, v2, v3
	v_cvt_pk_bf16_f32 v3, v4, v5
	v_cvt_pk_bf16_f32 v5, v8, v9
	v_add_co_u32_e32 v8, vcc, s60, v150
	v_cvt_pk_bf16_f32 v4, v10, v11
	s_nop 0
	v_addc_co_u32_e32 v9, vcc, 0, v151, vcc
	global_store_dwordx4 v[8:9], v[2:5], off
	v_pk_add_f32 v[8:9], v[116:117], v[132:133]
	v_pk_add_f32 v[10:11], v[114:115], v[130:131]
	v_pk_add_f32 v[4:5], v[120:121], v[136:137]
	v_pk_add_f32 v[2:3], v[118:119], v[134:135]
	s_nop 0
	v_cvt_pk_bf16_f32 v2, v2, v3
	v_cvt_pk_bf16_f32 v3, v4, v5
	v_cvt_pk_bf16_f32 v4, v10, v11
	v_cvt_pk_bf16_f32 v5, v8, v9
	global_store_dwordx4 v[6:7], v[2:5], off offset:256
	v_pk_add_f32 v[8:9], v[108:109], v[140:141]
	v_pk_add_f32 v[10:11], v[106:107], v[138:139]
	v_pk_add_f32 v[4:5], v[112:113], v[144:145]
	v_pk_add_f32 v[2:3], v[110:111], v[142:143]
	v_lshl_add_u64 v[6:7], v[150:151], 0, s[20:21]
	v_cvt_pk_bf16_f32 v2, v2, v3
	v_cvt_pk_bf16_f32 v3, v4, v5
	v_cvt_pk_bf16_f32 v5, v8, v9
	v_add_co_u32_e32 v8, vcc, s69, v150
	v_cvt_pk_bf16_f32 v4, v10, v11
	s_nop 0
	v_addc_co_u32_e32 v9, vcc, 0, v151, vcc
	global_store_dwordx4 v[8:9], v[2:5], off
	v_pk_add_f32 v[8:9], v[100:101], v[132:133]
	v_pk_add_f32 v[10:11], v[98:99], v[130:131]
	v_pk_add_f32 v[4:5], v[104:105], v[136:137]
	v_pk_add_f32 v[2:3], v[102:103], v[134:135]
	s_nop 0
	v_cvt_pk_bf16_f32 v2, v2, v3
	v_cvt_pk_bf16_f32 v3, v4, v5
	v_cvt_pk_bf16_f32 v4, v10, v11
	v_cvt_pk_bf16_f32 v5, v8, v9
	global_store_dwordx4 v[6:7], v[2:5], off offset:256
	v_pk_add_f32 v[8:9], v[92:93], v[140:141]
	v_pk_add_f32 v[10:11], v[90:91], v[138:139]
	v_pk_add_f32 v[4:5], v[96:97], v[144:145]
	v_pk_add_f32 v[2:3], v[94:95], v[142:143]
	v_lshl_add_u64 v[6:7], v[150:151], 0, s[22:23]
	v_cvt_pk_bf16_f32 v2, v2, v3
	v_cvt_pk_bf16_f32 v3, v4, v5
	v_cvt_pk_bf16_f32 v5, v8, v9
	v_add_co_u32_e32 v8, vcc, s70, v150
	v_cvt_pk_bf16_f32 v4, v10, v11
	s_nop 0
	v_addc_co_u32_e32 v9, vcc, 0, v151, vcc
	global_store_dwordx4 v[8:9], v[2:5], off
	v_pk_add_f32 v[8:9], v[84:85], v[132:133]
	v_pk_add_f32 v[10:11], v[82:83], v[130:131]
	v_pk_add_f32 v[4:5], v[88:89], v[136:137]
	v_pk_add_f32 v[2:3], v[86:87], v[134:135]
	s_nop 0
	v_cvt_pk_bf16_f32 v2, v2, v3
	v_cvt_pk_bf16_f32 v3, v4, v5
	v_cvt_pk_bf16_f32 v4, v10, v11
	v_cvt_pk_bf16_f32 v5, v8, v9
	global_store_dwordx4 v[6:7], v[2:5], off offset:256
	v_pk_add_f32 v[8:9], v[76:77], v[140:141]
	v_pk_add_f32 v[10:11], v[74:75], v[138:139]
	v_pk_add_f32 v[4:5], v[80:81], v[144:145]
	v_pk_add_f32 v[2:3], v[78:79], v[142:143]
	v_lshl_add_u64 v[6:7], v[150:151], 0, s[24:25]
	v_cvt_pk_bf16_f32 v2, v2, v3
	v_cvt_pk_bf16_f32 v3, v4, v5
	v_cvt_pk_bf16_f32 v5, v8, v9
	v_add_co_u32_e32 v8, vcc, s71, v150
	v_cvt_pk_bf16_f32 v4, v10, v11
	s_nop 0
	v_addc_co_u32_e32 v9, vcc, 0, v151, vcc
	global_store_dwordx4 v[8:9], v[2:5], off
	v_pk_add_f32 v[8:9], v[68:69], v[132:133]
	v_pk_add_f32 v[10:11], v[66:67], v[130:131]
	v_pk_add_f32 v[4:5], v[72:73], v[136:137]
	v_pk_add_f32 v[2:3], v[70:71], v[134:135]
	s_andn2_b64 vcc, exec, s[38:39]
	v_cvt_pk_bf16_f32 v2, v2, v3
	v_cvt_pk_bf16_f32 v3, v4, v5
	v_cvt_pk_bf16_f32 v4, v10, v11
	v_cvt_pk_bf16_f32 v5, v8, v9
	global_store_dwordx4 v[6:7], v[2:5], off offset:256
	s_cbranch_vccnz .LBB0_1446
	s_ashr_i32 s31, s30, 31
	s_lshl_b32 s10, s26, 8
	v_readlane_b32 s44, v246, 0
	s_ashr_i32 s11, s10, 31
	s_lshl_b64 s[38:39], s[30:31], 13
	v_readlane_b32 s46, v246, 2
	v_readlane_b32 s47, v246, 3
	s_add_u32 s27, s46, s38
	s_addc_u32 s31, s47, s39
	s_lshl_b64 s[10:11], s[10:11], 2
	s_add_u32 s10, s27, s10
	s_addc_u32 s11, s31, s11
	s_add_u32 s10, s10, s41
	s_addc_u32 s11, s11, 0
	v_lshl_add_u64 v[2:3], s[10:11], 0, v[146:147]
	v_mov_b32_e32 v149, v147
	v_lshl_add_u64 v[2:3], v[2:3], 0, v[148:149]
	global_load_dword v130, v[2:3], off
	s_andn2_b64 vcc, exec, s[12:13]
	v_readlane_b32 s45, v246, 1
	v_readlane_b32 s48, v246, 4
	v_readlane_b32 s49, v246, 5
	v_readlane_b32 s50, v246, 6
	v_readlane_b32 s51, v246, 7
	s_cbranch_vccnz .LBB0_1445
	s_barrier
	s_branch .LBB0_1445
